# out-proj epilogue: the 14 gate-row loads of rows 0..6 issued together up front instead of one load + vmcnt(0) per position
# speedup vs baseline: 1.0223x; 1.0010x over previous
.LBB0_1203:
	s_lshr_b64 s[54:55], s[52:53], 24
	s_and_b32 s1, s54, 0xffffff00
	v_lshl_add_u32 v4, s52, 8, v1
	v_or_b32_e32 v2, s1, v179
	v_mad_i64_i32 v[10:11], s[52:53], v4, s73, 0
	v_lshl_add_u64 v[6:7], v[10:11], 1, s[12:13]
	v_ashrrev_i32_e32 v3, 31, v2
	v_lshl_add_u64 v[8:9], v[2:3], 1, v[6:7]
	s_nop 15
	s_nop 15
	s_nop 15
	s_nop 15
	v_mad_i64_i32 v[254:255], s[98:99], v4, s73, 0
	v_lshl_add_u64 v[254:255], v[254:255], 1, s[12:13]
	v_lshl_add_u64 v[254:255], v[2:3], 1, v[254:255]
	global_load_dwordx4 v[196:199], v[254:255], off
	global_load_dwordx4 v[200:203], v[254:255], off offset:256
	v_or_b32_e32 v254, 16, v4
	v_mad_i64_i32 v[254:255], s[98:99], v254, s73, 0
	v_lshl_add_u64 v[254:255], v[254:255], 1, s[12:13]
	v_lshl_add_u64 v[254:255], v[2:3], 1, v[254:255]
	global_load_dwordx4 v[204:207], v[254:255], off
	global_load_dwordx4 v[208:211], v[254:255], off offset:256
	v_or_b32_e32 v254, 32, v4
	v_mad_i64_i32 v[254:255], s[98:99], v254, s73, 0
	v_lshl_add_u64 v[254:255], v[254:255], 1, s[12:13]
	v_lshl_add_u64 v[254:255], v[2:3], 1, v[254:255]
	global_load_dwordx4 v[212:215], v[254:255], off
	global_load_dwordx4 v[216:219], v[254:255], off offset:256
	v_or_b32_e32 v254, 48, v4
	v_mad_i64_i32 v[254:255], s[98:99], v254, s73, 0
	v_lshl_add_u64 v[254:255], v[254:255], 1, s[12:13]
	v_lshl_add_u64 v[254:255], v[2:3], 1, v[254:255]
	global_load_dwordx4 v[220:223], v[254:255], off
	global_load_dwordx4 v[224:227], v[254:255], off offset:256
	v_add_u32_e32 v254, 0x80, v4
	v_mad_i64_i32 v[254:255], s[98:99], v254, s73, 0
	v_lshl_add_u64 v[254:255], v[254:255], 1, s[12:13]
	v_lshl_add_u64 v[254:255], v[2:3], 1, v[254:255]
	global_load_dwordx4 v[182:185], v[254:255], off
	global_load_dwordx4 v[186:189], v[254:255], off offset:256
	v_add_u32_e32 v254, 0x90, v4
	v_mad_i64_i32 v[254:255], s[98:99], v254, s73, 0
	v_lshl_add_u64 v[254:255], v[254:255], 1, s[12:13]
	v_lshl_add_u64 v[254:255], v[2:3], 1, v[254:255]
	global_load_dwordx4 v[238:241], v[254:255], off
	global_load_dwordx4 v[242:245], v[254:255], off offset:256
	v_add_u32_e32 v254, 0xa0, v4
	v_mad_i64_i32 v[254:255], s[98:99], v254, s73, 0
	v_lshl_add_u64 v[254:255], v[254:255], 1, s[12:13]
	v_lshl_add_u64 v[254:255], v[2:3], 1, v[254:255]
	global_load_dwordx4 v[246:249], v[254:255], off
	global_load_dwordx4 v[250:253], v[254:255], off offset:256
	v_ashrrev_i32_e32 v5, 31, v4
	v_lshlrev_b64 v[6:7], 11, v[4:5]
	s_cmp_lg_u32 s0, 0
	v_lshl_add_u64 v[6:7], s[4:5], 0, v[6:7]
	s_cselect_b64 s[52:53], -1, 0
	s_cmp_eq_u32 s0, 0
	v_lshl_add_u64 v[6:7], v[6:7], 0, v[2:3]
	s_waitcnt vmcnt(0)
	v_lshlrev_b32_e32 v18, 16, v196
	v_and_b32_e32 v17, 0xffff0000, v196
	v_lshlrev_b32_e32 v16, 16, v197
	v_and_b32_e32 v15, 0xffff0000, v197
	v_lshlrev_b32_e32 v14, 16, v198
	v_and_b32_e32 v13, 0xffff0000, v198
	v_lshlrev_b32_e32 v12, 16, v199
	v_and_b32_e32 v5, 0xffff0000, v199
	s_cbranch_scc1 .LBB0_1256
	v_mul_f32_e32 v19, 0xbfb8aa3b, v18
	v_mul_f32_e32 v20, 0xbfb8aa3b, v17
	v_exp_f32_e32 v19, v19
	v_mul_f32_e32 v21, 0xbfb8aa3b, v16
	v_exp_f32_e32 v20, v20
	v_mul_f32_e32 v23, 0xbfb8aa3b, v14
	v_mul_f32_e32 v24, 0xbfb8aa3b, v13
	v_exp_f32_e32 v21, v21
	v_exp_f32_e32 v23, v23
	v_exp_f32_e32 v24, v24
	v_mul_f32_e32 v22, 0xbfb8aa3b, v15
	v_add_f32_e32 v19, 1.0, v19
	v_add_f32_e32 v20, 1.0, v20
	v_exp_f32_e32 v22, v22
	v_mul_f32_e32 v25, 0xbfb8aa3b, v12
	v_mul_f32_e32 v27, 0xbfb8aa3b, v5
	v_rcp_f32_e32 v19, v19
	v_rcp_f32_e32 v20, v20
	v_add_f32_e32 v21, 1.0, v21
	v_add_f32_e32 v23, 1.0, v23
	v_add_f32_e32 v24, 1.0, v24
	v_exp_f32_e32 v25, v25
	v_exp_f32_e32 v27, v27
	v_rcp_f32_e32 v21, v21
	v_rcp_f32_e32 v23, v23
	v_rcp_f32_e32 v24, v24
	v_add_f32_e32 v22, 1.0, v22
	v_mul_f32_e32 v19, v154, v19
	v_mul_f32_e32 v20, v155, v20
	v_rcp_f32_e32 v22, v22
	v_add_f32_e32 v25, 1.0, v25
	v_add_f32_e32 v27, 1.0, v27
	v_mul_f32_e32 v21, v156, v21
	v_rcp_f32_e32 v25, v25
	v_rcp_f32_e32 v27, v27
	v_mul_f32_e32 v23, v150, v23
	v_mul_f32_e32 v24, v151, v24
	v_mul_f32_e32 v19, 0x3c000000, v19
	v_mul_f32_e32 v28, 0x3c000000, v20
	v_mov_b32_e32 v20, 0
	v_mul_f32_e32 v29, 0x3c000000, v21
	v_cvt_pk_fp8_f32 v20, v19, v28
	v_mul_f32_e32 v19, 0x3c000000, v23
	v_mul_f32_e32 v23, 0x3c000000, v24
	v_mov_b32_e32 v21, 0
	v_cvt_pk_fp8_f32 v21, v19, v23
	v_mul_f32_e32 v22, v157, v22
	v_mul_f32_e32 v25, v152, v25
	v_mul_f32_e32 v27, v153, v27
	v_mul_f32_e32 v22, 0x3c000000, v22
	v_cvt_pk_fp8_f32 v20, v29, v22 op_sel:[0,0,1]
	v_mul_f32_e32 v19, 0x3c000000, v25
	v_mul_f32_e32 v22, 0x3c000000, v27
	v_cvt_pk_fp8_f32 v21, v19, v22 op_sel:[0,0,1]
	global_store_dwordx2 v[6:7], v[20:21], off
	v_lshl_add_u64 v[10:11], v[10:11], 1, s[10:11]
	s_cbranch_execnz .LBB0_1206

.LBB0_1206:
	v_cndmask_b32_e64 v5, 0, 1, s[52:53]
	v_cmp_ne_u32_e64 s[0:1], 1, v5
	s_andn2_b64 vcc, exec, s[52:53]
	v_lshlrev_b32_e32 v16, 16, v200
	v_and_b32_e32 v15, 0xffff0000, v200
	v_lshlrev_b32_e32 v14, 16, v201
	v_and_b32_e32 v13, 0xffff0000, v201
	v_lshlrev_b32_e32 v12, 16, v202
	v_and_b32_e32 v9, 0xffff0000, v202
	v_lshlrev_b32_e32 v8, 16, v203
	v_and_b32_e32 v5, 0xffff0000, v203
	s_cbranch_vccnz .LBB0_1257
	v_mul_f32_e32 v17, 0xbfb8aa3b, v16
	v_mul_f32_e32 v18, 0xbfb8aa3b, v15
	v_exp_f32_e32 v17, v17
	v_mul_f32_e32 v19, 0xbfb8aa3b, v14
	v_exp_f32_e32 v18, v18
	v_mul_f32_e32 v21, 0xbfb8aa3b, v12
	v_mul_f32_e32 v22, 0xbfb8aa3b, v9
	v_exp_f32_e32 v19, v19
	v_exp_f32_e32 v21, v21
	v_exp_f32_e32 v22, v22
	v_mul_f32_e32 v20, 0xbfb8aa3b, v13
	v_add_f32_e32 v17, 1.0, v17
	v_add_f32_e32 v18, 1.0, v18
	v_exp_f32_e32 v20, v20
	v_mul_f32_e32 v23, 0xbfb8aa3b, v8
	v_mul_f32_e32 v24, 0xbfb8aa3b, v5
	v_rcp_f32_e32 v17, v17
	v_rcp_f32_e32 v18, v18
	v_add_f32_e32 v19, 1.0, v19
	v_add_f32_e32 v21, 1.0, v21
	v_add_f32_e32 v22, 1.0, v22
	v_exp_f32_e32 v23, v23
	v_exp_f32_e32 v24, v24
	v_rcp_f32_e32 v19, v19
	v_rcp_f32_e32 v21, v21
	v_rcp_f32_e32 v22, v22
	v_add_f32_e32 v20, 1.0, v20
	v_mul_f32_e32 v17, v122, v17
	v_mul_f32_e32 v18, v123, v18
	v_rcp_f32_e32 v20, v20
	v_add_f32_e32 v23, 1.0, v23
	v_add_f32_e32 v24, 1.0, v24
	v_mul_f32_e32 v19, v124, v19
	v_rcp_f32_e32 v23, v23
	v_rcp_f32_e32 v24, v24
	v_mul_f32_e32 v21, v118, v21
	v_mul_f32_e32 v22, v119, v22
	v_mul_f32_e32 v17, 0x3c000000, v17
	v_mul_f32_e32 v25, 0x3c000000, v18
	v_mov_b32_e32 v18, 0
	v_mul_f32_e32 v27, 0x3c000000, v19
	v_cvt_pk_fp8_f32 v18, v17, v25
	v_mul_f32_e32 v17, 0x3c000000, v21
	v_mul_f32_e32 v21, 0x3c000000, v22
	v_mov_b32_e32 v19, 0
	v_cvt_pk_fp8_f32 v19, v17, v21
	v_mul_f32_e32 v20, v125, v20
	v_mul_f32_e32 v23, v120, v23
	v_mul_f32_e32 v24, v121, v24
	v_mul_f32_e32 v20, 0x3c000000, v20
	v_cvt_pk_fp8_f32 v18, v27, v20 op_sel:[0,0,1]
	v_mul_f32_e32 v17, 0x3c000000, v23
	v_mul_f32_e32 v20, 0x3c000000, v24
	v_cvt_pk_fp8_f32 v19, v17, v20 op_sel:[0,0,1]
	global_store_dwordx2 v[6:7], v[18:19], off offset:128
	s_cbranch_execnz .LBB0_1209

.LBB0_1209:
	v_or_b32_e32 v6, 16, v4
	v_mad_i64_i32 v[10:11], s[52:53], v6, s73, 0
	v_lshl_add_u64 v[8:9], v[10:11], 1, s[12:13]
	v_lshl_add_u64 v[8:9], v[2:3], 1, v[8:9]
	v_ashrrev_i32_e32 v7, 31, v6
	v_lshlrev_b64 v[6:7], 11, v[6:7]
	v_lshl_add_u64 v[6:7], s[4:5], 0, v[6:7]
	s_and_b64 vcc, exec, s[0:1]
	v_lshl_add_u64 v[6:7], v[6:7], 0, v[2:3]
	v_lshlrev_b32_e32 v18, 16, v204
	v_and_b32_e32 v17, 0xffff0000, v204
	v_lshlrev_b32_e32 v16, 16, v205
	v_and_b32_e32 v15, 0xffff0000, v205
	v_lshlrev_b32_e32 v14, 16, v206
	v_and_b32_e32 v13, 0xffff0000, v206
	v_lshlrev_b32_e32 v12, 16, v207
	v_and_b32_e32 v5, 0xffff0000, v207
	s_cbranch_vccnz .LBB0_1258
	v_mul_f32_e32 v19, 0xbfb8aa3b, v18
	v_mul_f32_e32 v20, 0xbfb8aa3b, v17
	v_exp_f32_e32 v19, v19
	v_mul_f32_e32 v21, 0xbfb8aa3b, v16
	v_exp_f32_e32 v20, v20
	v_mul_f32_e32 v23, 0xbfb8aa3b, v14
	v_mul_f32_e32 v24, 0xbfb8aa3b, v13
	v_exp_f32_e32 v21, v21
	v_exp_f32_e32 v23, v23
	v_exp_f32_e32 v24, v24
	v_mul_f32_e32 v22, 0xbfb8aa3b, v15
	v_add_f32_e32 v19, 1.0, v19
	v_add_f32_e32 v20, 1.0, v20
	v_exp_f32_e32 v22, v22
	v_mul_f32_e32 v25, 0xbfb8aa3b, v12
	v_mul_f32_e32 v27, 0xbfb8aa3b, v5
	v_rcp_f32_e32 v19, v19
	v_rcp_f32_e32 v20, v20
	v_add_f32_e32 v21, 1.0, v21
	v_add_f32_e32 v23, 1.0, v23
	v_add_f32_e32 v24, 1.0, v24
	v_exp_f32_e32 v25, v25
	v_exp_f32_e32 v27, v27
	v_rcp_f32_e32 v21, v21
	v_rcp_f32_e32 v23, v23
	v_rcp_f32_e32 v24, v24
	v_add_f32_e32 v22, 1.0, v22
	v_mul_f32_e32 v19, v146, v19
	v_mul_f32_e32 v20, v147, v20
	v_rcp_f32_e32 v22, v22
	v_add_f32_e32 v25, 1.0, v25
	v_add_f32_e32 v27, 1.0, v27
	v_mul_f32_e32 v21, v148, v21
	v_rcp_f32_e32 v25, v25
	v_rcp_f32_e32 v27, v27
	v_mul_f32_e32 v23, v142, v23
	v_mul_f32_e32 v24, v143, v24
	v_mul_f32_e32 v19, 0x3c000000, v19
	v_mul_f32_e32 v28, 0x3c000000, v20
	v_mov_b32_e32 v20, 0
	v_mul_f32_e32 v29, 0x3c000000, v21
	v_cvt_pk_fp8_f32 v20, v19, v28
	v_mul_f32_e32 v19, 0x3c000000, v23
	v_mul_f32_e32 v23, 0x3c000000, v24
	v_mov_b32_e32 v21, 0
	v_cvt_pk_fp8_f32 v21, v19, v23
	v_mul_f32_e32 v22, v149, v22
	v_mul_f32_e32 v25, v144, v25
	v_mul_f32_e32 v27, v145, v27
	v_mul_f32_e32 v22, 0x3c000000, v22
	v_cvt_pk_fp8_f32 v20, v29, v22 op_sel:[0,0,1]
	v_mul_f32_e32 v19, 0x3c000000, v25
	v_mul_f32_e32 v22, 0x3c000000, v27
	v_cvt_pk_fp8_f32 v21, v19, v22 op_sel:[0,0,1]
	global_store_dwordx2 v[6:7], v[20:21], off
	v_lshl_add_u64 v[10:11], v[10:11], 1, s[10:11]
	s_cbranch_execnz .LBB0_1212

.LBB0_1212:
	s_and_b64 vcc, exec, s[0:1]
	v_lshlrev_b32_e32 v16, 16, v208
	v_and_b32_e32 v15, 0xffff0000, v208
	v_lshlrev_b32_e32 v14, 16, v209
	v_and_b32_e32 v13, 0xffff0000, v209
	v_lshlrev_b32_e32 v12, 16, v210
	v_and_b32_e32 v9, 0xffff0000, v210
	v_lshlrev_b32_e32 v8, 16, v211
	v_and_b32_e32 v5, 0xffff0000, v211
	s_cbranch_vccnz .LBB0_1259
	v_mul_f32_e32 v17, 0xbfb8aa3b, v16
	v_mul_f32_e32 v18, 0xbfb8aa3b, v15
	v_exp_f32_e32 v17, v17
	v_mul_f32_e32 v19, 0xbfb8aa3b, v14
	v_exp_f32_e32 v18, v18
	v_mul_f32_e32 v21, 0xbfb8aa3b, v12
	v_mul_f32_e32 v22, 0xbfb8aa3b, v9
	v_exp_f32_e32 v19, v19
	v_exp_f32_e32 v21, v21
	v_exp_f32_e32 v22, v22
	v_mul_f32_e32 v20, 0xbfb8aa3b, v13
	v_add_f32_e32 v17, 1.0, v17
	v_add_f32_e32 v18, 1.0, v18
	v_exp_f32_e32 v20, v20
	v_mul_f32_e32 v23, 0xbfb8aa3b, v8
	v_mul_f32_e32 v24, 0xbfb8aa3b, v5
	v_rcp_f32_e32 v17, v17
	v_rcp_f32_e32 v18, v18
	v_add_f32_e32 v19, 1.0, v19
	v_add_f32_e32 v21, 1.0, v21
	v_add_f32_e32 v22, 1.0, v22
	v_exp_f32_e32 v23, v23
	v_exp_f32_e32 v24, v24
	v_rcp_f32_e32 v19, v19
	v_rcp_f32_e32 v21, v21
	v_rcp_f32_e32 v22, v22
	v_add_f32_e32 v20, 1.0, v20
	v_mul_f32_e32 v17, v114, v17
	v_mul_f32_e32 v18, v115, v18
	v_rcp_f32_e32 v20, v20
	v_add_f32_e32 v23, 1.0, v23
	v_add_f32_e32 v24, 1.0, v24
	v_mul_f32_e32 v19, v116, v19
	v_rcp_f32_e32 v23, v23
	v_rcp_f32_e32 v24, v24
	v_mul_f32_e32 v21, v110, v21
	v_mul_f32_e32 v22, v111, v22
	v_mul_f32_e32 v17, 0x3c000000, v17
	v_mul_f32_e32 v25, 0x3c000000, v18
	v_mov_b32_e32 v18, 0
	v_mul_f32_e32 v27, 0x3c000000, v19
	v_cvt_pk_fp8_f32 v18, v17, v25
	v_mul_f32_e32 v17, 0x3c000000, v21
	v_mul_f32_e32 v21, 0x3c000000, v22
	v_mov_b32_e32 v19, 0
	v_cvt_pk_fp8_f32 v19, v17, v21
	v_mul_f32_e32 v20, v117, v20
	v_mul_f32_e32 v23, v112, v23
	v_mul_f32_e32 v24, v113, v24
	v_mul_f32_e32 v20, 0x3c000000, v20
	v_cvt_pk_fp8_f32 v18, v27, v20 op_sel:[0,0,1]
	v_mul_f32_e32 v17, 0x3c000000, v23
	v_mul_f32_e32 v20, 0x3c000000, v24
	v_cvt_pk_fp8_f32 v19, v17, v20 op_sel:[0,0,1]
	global_store_dwordx2 v[6:7], v[18:19], off offset:128
	s_cbranch_execnz .LBB0_1215

.LBB0_1215:
	v_or_b32_e32 v6, 32, v4
	v_mad_i64_i32 v[10:11], s[52:53], v6, s73, 0
	v_lshl_add_u64 v[8:9], v[10:11], 1, s[12:13]
	v_lshl_add_u64 v[8:9], v[2:3], 1, v[8:9]
	v_ashrrev_i32_e32 v7, 31, v6
	v_lshlrev_b64 v[6:7], 11, v[6:7]
	v_lshl_add_u64 v[6:7], s[4:5], 0, v[6:7]
	s_and_b64 vcc, exec, s[0:1]
	v_lshl_add_u64 v[6:7], v[6:7], 0, v[2:3]
	v_lshlrev_b32_e32 v18, 16, v212
	v_and_b32_e32 v17, 0xffff0000, v212
	v_lshlrev_b32_e32 v16, 16, v213
	v_and_b32_e32 v15, 0xffff0000, v213
	v_lshlrev_b32_e32 v14, 16, v214
	v_and_b32_e32 v13, 0xffff0000, v214
	v_lshlrev_b32_e32 v12, 16, v215
	v_and_b32_e32 v5, 0xffff0000, v215
	s_cbranch_vccnz .LBB0_1260
	v_mul_f32_e32 v19, 0xbfb8aa3b, v18
	v_mul_f32_e32 v20, 0xbfb8aa3b, v17
	v_exp_f32_e32 v19, v19
	v_mul_f32_e32 v21, 0xbfb8aa3b, v16
	v_exp_f32_e32 v20, v20
	v_mul_f32_e32 v23, 0xbfb8aa3b, v14
	v_mul_f32_e32 v24, 0xbfb8aa3b, v13
	v_exp_f32_e32 v21, v21
	v_exp_f32_e32 v23, v23
	v_exp_f32_e32 v24, v24
	v_mul_f32_e32 v22, 0xbfb8aa3b, v15
	v_add_f32_e32 v19, 1.0, v19
	v_add_f32_e32 v20, 1.0, v20
	v_exp_f32_e32 v22, v22
	v_mul_f32_e32 v25, 0xbfb8aa3b, v12
	v_mul_f32_e32 v27, 0xbfb8aa3b, v5
	v_rcp_f32_e32 v19, v19
	v_rcp_f32_e32 v20, v20
	v_add_f32_e32 v21, 1.0, v21
	v_add_f32_e32 v23, 1.0, v23
	v_add_f32_e32 v24, 1.0, v24
	v_exp_f32_e32 v25, v25
	v_exp_f32_e32 v27, v27
	v_rcp_f32_e32 v21, v21
	v_rcp_f32_e32 v23, v23
	v_rcp_f32_e32 v24, v24
	v_add_f32_e32 v22, 1.0, v22
	v_mul_f32_e32 v19, v138, v19
	v_mul_f32_e32 v20, v139, v20
	v_rcp_f32_e32 v22, v22
	v_add_f32_e32 v25, 1.0, v25
	v_add_f32_e32 v27, 1.0, v27
	v_mul_f32_e32 v21, v140, v21
	v_rcp_f32_e32 v25, v25
	v_rcp_f32_e32 v27, v27
	v_mul_f32_e32 v23, v134, v23
	v_mul_f32_e32 v24, v135, v24
	v_mul_f32_e32 v19, 0x3c000000, v19
	v_mul_f32_e32 v28, 0x3c000000, v20
	v_mov_b32_e32 v20, 0
	v_mul_f32_e32 v29, 0x3c000000, v21
	v_cvt_pk_fp8_f32 v20, v19, v28
	v_mul_f32_e32 v19, 0x3c000000, v23
	v_mul_f32_e32 v23, 0x3c000000, v24
	v_mov_b32_e32 v21, 0
	v_cvt_pk_fp8_f32 v21, v19, v23
	v_mul_f32_e32 v22, v141, v22
	v_mul_f32_e32 v25, v136, v25
	v_mul_f32_e32 v27, v137, v27
	v_mul_f32_e32 v22, 0x3c000000, v22
	v_cvt_pk_fp8_f32 v20, v29, v22 op_sel:[0,0,1]
	v_mul_f32_e32 v19, 0x3c000000, v25
	v_mul_f32_e32 v22, 0x3c000000, v27
	v_cvt_pk_fp8_f32 v21, v19, v22 op_sel:[0,0,1]
	global_store_dwordx2 v[6:7], v[20:21], off
	v_lshl_add_u64 v[10:11], v[10:11], 1, s[10:11]
	s_cbranch_execnz .LBB0_1218

.LBB0_1218:
	s_and_b64 vcc, exec, s[0:1]
	v_lshlrev_b32_e32 v16, 16, v216
	v_and_b32_e32 v15, 0xffff0000, v216
	v_lshlrev_b32_e32 v14, 16, v217
	v_and_b32_e32 v13, 0xffff0000, v217
	v_lshlrev_b32_e32 v12, 16, v218
	v_and_b32_e32 v9, 0xffff0000, v218
	v_lshlrev_b32_e32 v8, 16, v219
	v_and_b32_e32 v5, 0xffff0000, v219
	s_cbranch_vccnz .LBB0_1261
	v_mul_f32_e32 v17, 0xbfb8aa3b, v16
	v_mul_f32_e32 v18, 0xbfb8aa3b, v15
	v_exp_f32_e32 v17, v17
	v_mul_f32_e32 v19, 0xbfb8aa3b, v14
	v_exp_f32_e32 v18, v18
	v_mul_f32_e32 v21, 0xbfb8aa3b, v12
	v_mul_f32_e32 v22, 0xbfb8aa3b, v9
	v_exp_f32_e32 v19, v19
	v_exp_f32_e32 v21, v21
	v_exp_f32_e32 v22, v22
	v_mul_f32_e32 v20, 0xbfb8aa3b, v13
	v_add_f32_e32 v17, 1.0, v17
	v_add_f32_e32 v18, 1.0, v18
	v_exp_f32_e32 v20, v20
	v_mul_f32_e32 v23, 0xbfb8aa3b, v8
	v_mul_f32_e32 v24, 0xbfb8aa3b, v5
	v_rcp_f32_e32 v17, v17
	v_rcp_f32_e32 v18, v18
	v_add_f32_e32 v19, 1.0, v19
	v_add_f32_e32 v21, 1.0, v21
	v_add_f32_e32 v22, 1.0, v22
	v_exp_f32_e32 v23, v23
	v_exp_f32_e32 v24, v24
	v_rcp_f32_e32 v19, v19
	v_rcp_f32_e32 v21, v21
	v_rcp_f32_e32 v22, v22
	v_add_f32_e32 v20, 1.0, v20
	v_mul_f32_e32 v17, v106, v17
	v_mul_f32_e32 v18, v107, v18
	v_rcp_f32_e32 v20, v20
	v_add_f32_e32 v23, 1.0, v23
	v_add_f32_e32 v24, 1.0, v24
	v_mul_f32_e32 v19, v108, v19
	v_rcp_f32_e32 v23, v23
	v_rcp_f32_e32 v24, v24
	v_mul_f32_e32 v21, v102, v21
	v_mul_f32_e32 v22, v103, v22
	v_mul_f32_e32 v17, 0x3c000000, v17
	v_mul_f32_e32 v25, 0x3c000000, v18
	v_mov_b32_e32 v18, 0
	v_mul_f32_e32 v27, 0x3c000000, v19
	v_cvt_pk_fp8_f32 v18, v17, v25
	v_mul_f32_e32 v17, 0x3c000000, v21
	v_mul_f32_e32 v21, 0x3c000000, v22
	v_mov_b32_e32 v19, 0
	v_cvt_pk_fp8_f32 v19, v17, v21
	v_mul_f32_e32 v20, v109, v20
	v_mul_f32_e32 v23, v104, v23
	v_mul_f32_e32 v24, v105, v24
	v_mul_f32_e32 v20, 0x3c000000, v20
	v_cvt_pk_fp8_f32 v18, v27, v20 op_sel:[0,0,1]
	v_mul_f32_e32 v17, 0x3c000000, v23
	v_mul_f32_e32 v20, 0x3c000000, v24
	v_cvt_pk_fp8_f32 v19, v17, v20 op_sel:[0,0,1]
	global_store_dwordx2 v[6:7], v[18:19], off offset:128
	s_cbranch_execnz .LBB0_1221

.LBB0_1221:
	v_or_b32_e32 v6, 48, v4
	v_mad_i64_i32 v[10:11], s[52:53], v6, s73, 0
	v_lshl_add_u64 v[8:9], v[10:11], 1, s[12:13]
	v_lshl_add_u64 v[8:9], v[2:3], 1, v[8:9]
	v_ashrrev_i32_e32 v7, 31, v6
	v_lshlrev_b64 v[6:7], 11, v[6:7]
	v_lshl_add_u64 v[6:7], s[4:5], 0, v[6:7]
	s_and_b64 vcc, exec, s[0:1]
	v_lshl_add_u64 v[6:7], v[6:7], 0, v[2:3]
	v_lshlrev_b32_e32 v18, 16, v220
	v_and_b32_e32 v17, 0xffff0000, v220
	v_lshlrev_b32_e32 v16, 16, v221
	v_and_b32_e32 v15, 0xffff0000, v221
	v_lshlrev_b32_e32 v14, 16, v222
	v_and_b32_e32 v13, 0xffff0000, v222
	v_lshlrev_b32_e32 v12, 16, v223
	v_and_b32_e32 v5, 0xffff0000, v223
	s_cbranch_vccnz .LBB0_1262
	v_mul_f32_e32 v19, 0xbfb8aa3b, v18
	v_mul_f32_e32 v20, 0xbfb8aa3b, v17
	v_exp_f32_e32 v19, v19
	v_mul_f32_e32 v21, 0xbfb8aa3b, v16
	v_exp_f32_e32 v20, v20
	v_mul_f32_e32 v23, 0xbfb8aa3b, v14
	v_mul_f32_e32 v24, 0xbfb8aa3b, v13
	v_exp_f32_e32 v21, v21
	v_exp_f32_e32 v23, v23
	v_exp_f32_e32 v24, v24
	v_mul_f32_e32 v22, 0xbfb8aa3b, v15
	v_add_f32_e32 v19, 1.0, v19
	v_add_f32_e32 v20, 1.0, v20
	v_exp_f32_e32 v22, v22
	v_mul_f32_e32 v25, 0xbfb8aa3b, v12
	v_mul_f32_e32 v27, 0xbfb8aa3b, v5
	v_rcp_f32_e32 v19, v19
	v_rcp_f32_e32 v20, v20
	v_add_f32_e32 v21, 1.0, v21
	v_add_f32_e32 v23, 1.0, v23
	v_add_f32_e32 v24, 1.0, v24
	v_exp_f32_e32 v25, v25
	v_exp_f32_e32 v27, v27
	v_rcp_f32_e32 v21, v21
	v_rcp_f32_e32 v23, v23
	v_rcp_f32_e32 v24, v24
	v_add_f32_e32 v22, 1.0, v22
	v_mul_f32_e32 v19, v130, v19
	v_mul_f32_e32 v20, v131, v20
	v_rcp_f32_e32 v22, v22
	v_add_f32_e32 v25, 1.0, v25
	v_add_f32_e32 v27, 1.0, v27
	v_mul_f32_e32 v21, v132, v21
	v_rcp_f32_e32 v25, v25
	v_rcp_f32_e32 v27, v27
	v_mul_f32_e32 v23, v126, v23
	v_mul_f32_e32 v24, v127, v24
	v_mul_f32_e32 v19, 0x3c000000, v19
	v_mul_f32_e32 v28, 0x3c000000, v20
	v_mov_b32_e32 v20, 0
	v_mul_f32_e32 v29, 0x3c000000, v21
	v_cvt_pk_fp8_f32 v20, v19, v28
	v_mul_f32_e32 v19, 0x3c000000, v23
	v_mul_f32_e32 v23, 0x3c000000, v24
	v_mov_b32_e32 v21, 0
	v_cvt_pk_fp8_f32 v21, v19, v23
	v_mul_f32_e32 v22, v133, v22
	v_mul_f32_e32 v25, v128, v25
	v_mul_f32_e32 v27, v129, v27
	v_mul_f32_e32 v22, 0x3c000000, v22
	v_cvt_pk_fp8_f32 v20, v29, v22 op_sel:[0,0,1]
	v_mul_f32_e32 v19, 0x3c000000, v25
	v_mul_f32_e32 v22, 0x3c000000, v27
	v_cvt_pk_fp8_f32 v21, v19, v22 op_sel:[0,0,1]
	global_store_dwordx2 v[6:7], v[20:21], off
	v_lshl_add_u64 v[10:11], v[10:11], 1, s[10:11]
	s_cbranch_execnz .LBB0_1224

.LBB0_1224:
	s_and_b64 vcc, exec, s[0:1]
	v_lshlrev_b32_e32 v16, 16, v224
	v_and_b32_e32 v15, 0xffff0000, v224
	v_lshlrev_b32_e32 v14, 16, v225
	v_and_b32_e32 v13, 0xffff0000, v225
	v_lshlrev_b32_e32 v12, 16, v226
	v_and_b32_e32 v9, 0xffff0000, v226
	v_lshlrev_b32_e32 v8, 16, v227
	v_and_b32_e32 v5, 0xffff0000, v227
	s_cbranch_vccnz .LBB0_1263
	v_mul_f32_e32 v17, 0xbfb8aa3b, v16
	v_mul_f32_e32 v18, 0xbfb8aa3b, v15
	v_exp_f32_e32 v17, v17
	v_mul_f32_e32 v19, 0xbfb8aa3b, v14
	v_exp_f32_e32 v18, v18
	v_mul_f32_e32 v21, 0xbfb8aa3b, v12
	v_mul_f32_e32 v22, 0xbfb8aa3b, v9
	v_exp_f32_e32 v19, v19
	v_exp_f32_e32 v21, v21
	v_exp_f32_e32 v22, v22
	v_mul_f32_e32 v20, 0xbfb8aa3b, v13
	v_add_f32_e32 v17, 1.0, v17
	v_add_f32_e32 v18, 1.0, v18
	v_exp_f32_e32 v20, v20
	v_mul_f32_e32 v23, 0xbfb8aa3b, v8
	v_mul_f32_e32 v24, 0xbfb8aa3b, v5
	v_rcp_f32_e32 v17, v17
	v_rcp_f32_e32 v18, v18
	v_add_f32_e32 v19, 1.0, v19
	v_add_f32_e32 v21, 1.0, v21
	v_add_f32_e32 v22, 1.0, v22
	v_exp_f32_e32 v23, v23
	v_exp_f32_e32 v24, v24
	v_rcp_f32_e32 v19, v19
	v_rcp_f32_e32 v21, v21
	v_rcp_f32_e32 v22, v22
	v_add_f32_e32 v20, 1.0, v20
	v_mul_f32_e32 v17, v98, v17
	v_mul_f32_e32 v18, v99, v18
	v_rcp_f32_e32 v20, v20
	v_add_f32_e32 v23, 1.0, v23
	v_add_f32_e32 v24, 1.0, v24
	v_mul_f32_e32 v19, v100, v19
	v_rcp_f32_e32 v23, v23
	v_rcp_f32_e32 v24, v24
	v_mul_f32_e32 v21, v94, v21
	v_mul_f32_e32 v22, v95, v22
	v_mul_f32_e32 v17, 0x3c000000, v17
	v_mul_f32_e32 v25, 0x3c000000, v18
	v_mov_b32_e32 v18, 0
	v_mul_f32_e32 v27, 0x3c000000, v19
	v_cvt_pk_fp8_f32 v18, v17, v25
	v_mul_f32_e32 v17, 0x3c000000, v21
	v_mul_f32_e32 v21, 0x3c000000, v22
	v_mov_b32_e32 v19, 0
	v_cvt_pk_fp8_f32 v19, v17, v21
	v_mul_f32_e32 v20, v101, v20
	v_mul_f32_e32 v23, v96, v23
	v_mul_f32_e32 v24, v97, v24
	v_mul_f32_e32 v20, 0x3c000000, v20
	v_cvt_pk_fp8_f32 v18, v27, v20 op_sel:[0,0,1]
	v_mul_f32_e32 v17, 0x3c000000, v23
	v_mul_f32_e32 v20, 0x3c000000, v24
	v_cvt_pk_fp8_f32 v19, v17, v20 op_sel:[0,0,1]
	global_store_dwordx2 v[6:7], v[18:19], off offset:128
	s_cbranch_execnz .LBB0_1227

.LBB0_1227:
	v_add_u32_e32 v6, 0x80, v4
	v_mad_i64_i32 v[10:11], s[52:53], v6, s73, 0
	v_lshl_add_u64 v[8:9], v[10:11], 1, s[12:13]
	v_lshl_add_u64 v[8:9], v[2:3], 1, v[8:9]
	v_ashrrev_i32_e32 v7, 31, v6
	v_lshlrev_b64 v[6:7], 11, v[6:7]
	v_lshl_add_u64 v[6:7], s[4:5], 0, v[6:7]
	s_and_b64 vcc, exec, s[0:1]
	v_lshl_add_u64 v[6:7], v[6:7], 0, v[2:3]
	v_lshlrev_b32_e32 v18, 16, v182
	v_and_b32_e32 v17, 0xffff0000, v182
	v_lshlrev_b32_e32 v16, 16, v183
	v_and_b32_e32 v15, 0xffff0000, v183
	v_lshlrev_b32_e32 v14, 16, v184
	v_and_b32_e32 v13, 0xffff0000, v184
	v_lshlrev_b32_e32 v12, 16, v185
	v_and_b32_e32 v5, 0xffff0000, v185
	s_cbranch_vccnz .LBB0_1264
	v_mul_f32_e32 v19, 0xbfb8aa3b, v18
	v_mul_f32_e32 v20, 0xbfb8aa3b, v17
	v_exp_f32_e32 v19, v19
	v_mul_f32_e32 v21, 0xbfb8aa3b, v16
	v_exp_f32_e32 v20, v20
	v_mul_f32_e32 v23, 0xbfb8aa3b, v14
	v_mul_f32_e32 v24, 0xbfb8aa3b, v13
	v_exp_f32_e32 v21, v21
	v_exp_f32_e32 v23, v23
	v_exp_f32_e32 v24, v24
	v_mul_f32_e32 v22, 0xbfb8aa3b, v15
	v_add_f32_e32 v19, 1.0, v19
	v_add_f32_e32 v20, 1.0, v20
	v_exp_f32_e32 v22, v22
	v_mul_f32_e32 v25, 0xbfb8aa3b, v12
	v_mul_f32_e32 v27, 0xbfb8aa3b, v5
	v_rcp_f32_e32 v19, v19
	v_rcp_f32_e32 v20, v20
	v_add_f32_e32 v21, 1.0, v21
	v_add_f32_e32 v23, 1.0, v23
	v_add_f32_e32 v24, 1.0, v24
	v_exp_f32_e32 v25, v25
	v_exp_f32_e32 v27, v27
	v_rcp_f32_e32 v21, v21
	v_rcp_f32_e32 v23, v23
	v_rcp_f32_e32 v24, v24
	v_add_f32_e32 v22, 1.0, v22
	v_mul_f32_e32 v19, v90, v19
	v_mul_f32_e32 v20, v91, v20
	v_rcp_f32_e32 v22, v22
	v_add_f32_e32 v25, 1.0, v25
	v_add_f32_e32 v27, 1.0, v27
	v_mul_f32_e32 v21, v92, v21
	v_rcp_f32_e32 v25, v25
	v_rcp_f32_e32 v27, v27
	v_mul_f32_e32 v23, v86, v23
	v_mul_f32_e32 v24, v87, v24
	v_mul_f32_e32 v19, 0x3c000000, v19
	v_mul_f32_e32 v28, 0x3c000000, v20
	v_mov_b32_e32 v20, 0
	v_mul_f32_e32 v29, 0x3c000000, v21
	v_cvt_pk_fp8_f32 v20, v19, v28
	v_mul_f32_e32 v19, 0x3c000000, v23
	v_mul_f32_e32 v23, 0x3c000000, v24
	v_mov_b32_e32 v21, 0
	v_cvt_pk_fp8_f32 v21, v19, v23
	v_mul_f32_e32 v22, v93, v22
	v_mul_f32_e32 v25, v88, v25
	v_mul_f32_e32 v27, v89, v27
	v_mul_f32_e32 v22, 0x3c000000, v22
	v_cvt_pk_fp8_f32 v20, v29, v22 op_sel:[0,0,1]
	v_mul_f32_e32 v19, 0x3c000000, v25
	v_mul_f32_e32 v22, 0x3c000000, v27
	v_cvt_pk_fp8_f32 v21, v19, v22 op_sel:[0,0,1]
	global_store_dwordx2 v[6:7], v[20:21], off
	v_lshl_add_u64 v[10:11], v[10:11], 1, s[10:11]
	s_cbranch_execnz .LBB0_1230

.LBB0_1230:
	s_and_b64 vcc, exec, s[0:1]
	v_lshlrev_b32_e32 v16, 16, v186
	v_and_b32_e32 v15, 0xffff0000, v186
	v_lshlrev_b32_e32 v14, 16, v187
	v_and_b32_e32 v13, 0xffff0000, v187
	v_lshlrev_b32_e32 v12, 16, v188
	v_and_b32_e32 v9, 0xffff0000, v188
	v_lshlrev_b32_e32 v8, 16, v189
	v_and_b32_e32 v5, 0xffff0000, v189
	s_cbranch_vccnz .LBB0_1265
	v_mul_f32_e32 v17, 0xbfb8aa3b, v16
	v_mul_f32_e32 v18, 0xbfb8aa3b, v15
	v_exp_f32_e32 v17, v17
	v_mul_f32_e32 v19, 0xbfb8aa3b, v14
	v_exp_f32_e32 v18, v18
	v_mul_f32_e32 v21, 0xbfb8aa3b, v12
	v_mul_f32_e32 v22, 0xbfb8aa3b, v9
	v_exp_f32_e32 v19, v19
	v_exp_f32_e32 v21, v21
	v_exp_f32_e32 v22, v22
	v_mul_f32_e32 v20, 0xbfb8aa3b, v13
	v_add_f32_e32 v17, 1.0, v17
	v_add_f32_e32 v18, 1.0, v18
	v_exp_f32_e32 v20, v20
	v_mul_f32_e32 v23, 0xbfb8aa3b, v8
	v_mul_f32_e32 v24, 0xbfb8aa3b, v5
	v_rcp_f32_e32 v17, v17
	v_rcp_f32_e32 v18, v18
	v_add_f32_e32 v19, 1.0, v19
	v_add_f32_e32 v21, 1.0, v21
	v_add_f32_e32 v22, 1.0, v22
	v_exp_f32_e32 v23, v23
	v_exp_f32_e32 v24, v24
	v_rcp_f32_e32 v19, v19
	v_rcp_f32_e32 v21, v21
	v_rcp_f32_e32 v22, v22
	v_add_f32_e32 v20, 1.0, v20
	v_mul_f32_e32 v17, v58, v17
	v_mul_f32_e32 v18, v59, v18
	v_rcp_f32_e32 v20, v20
	v_add_f32_e32 v23, 1.0, v23
	v_add_f32_e32 v24, 1.0, v24
	v_mul_f32_e32 v19, v60, v19
	v_rcp_f32_e32 v23, v23
	v_rcp_f32_e32 v24, v24
	v_mul_f32_e32 v21, v54, v21
	v_mul_f32_e32 v22, v55, v22
	v_mul_f32_e32 v17, 0x3c000000, v17
	v_mul_f32_e32 v25, 0x3c000000, v18
	v_mov_b32_e32 v18, 0
	v_mul_f32_e32 v27, 0x3c000000, v19
	v_cvt_pk_fp8_f32 v18, v17, v25
	v_mul_f32_e32 v17, 0x3c000000, v21
	v_mul_f32_e32 v21, 0x3c000000, v22
	v_mov_b32_e32 v19, 0
	v_cvt_pk_fp8_f32 v19, v17, v21
	v_mul_f32_e32 v20, v61, v20
	v_mul_f32_e32 v23, v56, v23
	v_mul_f32_e32 v24, v57, v24
	v_mul_f32_e32 v20, 0x3c000000, v20
	v_cvt_pk_fp8_f32 v18, v27, v20 op_sel:[0,0,1]
	v_mul_f32_e32 v17, 0x3c000000, v23
	v_mul_f32_e32 v20, 0x3c000000, v24
	v_cvt_pk_fp8_f32 v19, v17, v20 op_sel:[0,0,1]
	global_store_dwordx2 v[6:7], v[18:19], off offset:128
	s_cbranch_execnz .LBB0_1233

.LBB0_1233:
	v_add_u32_e32 v6, 0x90, v4
	v_mad_i64_i32 v[10:11], s[52:53], v6, s73, 0
	v_lshl_add_u64 v[8:9], v[10:11], 1, s[12:13]
	v_lshl_add_u64 v[8:9], v[2:3], 1, v[8:9]
	v_ashrrev_i32_e32 v7, 31, v6
	v_lshlrev_b64 v[6:7], 11, v[6:7]
	v_lshl_add_u64 v[6:7], s[4:5], 0, v[6:7]
	s_and_b64 vcc, exec, s[0:1]
	v_lshl_add_u64 v[6:7], v[6:7], 0, v[2:3]
	v_lshlrev_b32_e32 v18, 16, v238
	v_and_b32_e32 v17, 0xffff0000, v238
	v_lshlrev_b32_e32 v16, 16, v239
	v_and_b32_e32 v15, 0xffff0000, v239
	v_lshlrev_b32_e32 v14, 16, v240
	v_and_b32_e32 v13, 0xffff0000, v240
	v_lshlrev_b32_e32 v12, 16, v241
	v_and_b32_e32 v5, 0xffff0000, v241
	s_cbranch_vccnz .LBB0_1266
	v_mul_f32_e32 v19, 0xbfb8aa3b, v18
	v_mul_f32_e32 v20, 0xbfb8aa3b, v17
	v_exp_f32_e32 v19, v19
	v_mul_f32_e32 v21, 0xbfb8aa3b, v16
	v_exp_f32_e32 v20, v20
	v_mul_f32_e32 v23, 0xbfb8aa3b, v14
	v_mul_f32_e32 v24, 0xbfb8aa3b, v13
	v_exp_f32_e32 v21, v21
	v_exp_f32_e32 v23, v23
	v_exp_f32_e32 v24, v24
	v_mul_f32_e32 v22, 0xbfb8aa3b, v15
	v_add_f32_e32 v19, 1.0, v19
	v_add_f32_e32 v20, 1.0, v20
	v_exp_f32_e32 v22, v22
	v_mul_f32_e32 v25, 0xbfb8aa3b, v12
	v_mul_f32_e32 v27, 0xbfb8aa3b, v5
	v_rcp_f32_e32 v19, v19
	v_rcp_f32_e32 v20, v20
	v_add_f32_e32 v21, 1.0, v21
	v_add_f32_e32 v23, 1.0, v23
	v_add_f32_e32 v24, 1.0, v24
	v_exp_f32_e32 v25, v25
	v_exp_f32_e32 v27, v27
	v_rcp_f32_e32 v21, v21
	v_rcp_f32_e32 v23, v23
	v_rcp_f32_e32 v24, v24
	v_add_f32_e32 v22, 1.0, v22
	v_mul_f32_e32 v19, v82, v19
	v_mul_f32_e32 v20, v83, v20
	v_rcp_f32_e32 v22, v22
	v_add_f32_e32 v25, 1.0, v25
	v_add_f32_e32 v27, 1.0, v27
	v_mul_f32_e32 v21, v84, v21
	v_rcp_f32_e32 v25, v25
	v_rcp_f32_e32 v27, v27
	v_mul_f32_e32 v23, v78, v23
	v_mul_f32_e32 v24, v79, v24
	v_mul_f32_e32 v19, 0x3c000000, v19
	v_mul_f32_e32 v28, 0x3c000000, v20
	v_mov_b32_e32 v20, 0
	v_mul_f32_e32 v29, 0x3c000000, v21
	v_cvt_pk_fp8_f32 v20, v19, v28
	v_mul_f32_e32 v19, 0x3c000000, v23
	v_mul_f32_e32 v23, 0x3c000000, v24
	v_mov_b32_e32 v21, 0
	v_cvt_pk_fp8_f32 v21, v19, v23
	v_mul_f32_e32 v22, v85, v22
	v_mul_f32_e32 v25, v80, v25
	v_mul_f32_e32 v27, v81, v27
	v_mul_f32_e32 v22, 0x3c000000, v22
	v_cvt_pk_fp8_f32 v20, v29, v22 op_sel:[0,0,1]
	v_mul_f32_e32 v19, 0x3c000000, v25
	v_mul_f32_e32 v22, 0x3c000000, v27
	v_cvt_pk_fp8_f32 v21, v19, v22 op_sel:[0,0,1]
	global_store_dwordx2 v[6:7], v[20:21], off
	v_lshl_add_u64 v[10:11], v[10:11], 1, s[10:11]
	s_cbranch_execnz .LBB0_1236

.LBB0_1236:
	s_and_b64 vcc, exec, s[0:1]
	v_lshlrev_b32_e32 v16, 16, v242
	v_and_b32_e32 v15, 0xffff0000, v242
	v_lshlrev_b32_e32 v14, 16, v243
	v_and_b32_e32 v13, 0xffff0000, v243
	v_lshlrev_b32_e32 v12, 16, v244
	v_and_b32_e32 v9, 0xffff0000, v244
	v_lshlrev_b32_e32 v8, 16, v245
	v_and_b32_e32 v5, 0xffff0000, v245
	s_cbranch_vccnz .LBB0_1267
	v_mul_f32_e32 v17, 0xbfb8aa3b, v16
	v_mul_f32_e32 v18, 0xbfb8aa3b, v15
	v_exp_f32_e32 v17, v17
	v_mul_f32_e32 v19, 0xbfb8aa3b, v14
	v_exp_f32_e32 v18, v18
	v_mul_f32_e32 v21, 0xbfb8aa3b, v12
	v_mul_f32_e32 v22, 0xbfb8aa3b, v9
	v_exp_f32_e32 v19, v19
	v_exp_f32_e32 v21, v21
	v_exp_f32_e32 v22, v22
	v_mul_f32_e32 v20, 0xbfb8aa3b, v13
	v_add_f32_e32 v17, 1.0, v17
	v_add_f32_e32 v18, 1.0, v18
	v_exp_f32_e32 v20, v20
	v_mul_f32_e32 v23, 0xbfb8aa3b, v8
	v_mul_f32_e32 v24, 0xbfb8aa3b, v5
	v_rcp_f32_e32 v17, v17
	v_rcp_f32_e32 v18, v18
	v_add_f32_e32 v19, 1.0, v19
	v_add_f32_e32 v21, 1.0, v21
	v_add_f32_e32 v22, 1.0, v22
	v_exp_f32_e32 v23, v23
	v_exp_f32_e32 v24, v24
	v_rcp_f32_e32 v19, v19
	v_rcp_f32_e32 v21, v21
	v_rcp_f32_e32 v22, v22
	v_add_f32_e32 v20, 1.0, v20
	v_mul_f32_e32 v17, v50, v17
	v_mul_f32_e32 v18, v51, v18
	v_rcp_f32_e32 v20, v20
	v_add_f32_e32 v23, 1.0, v23
	v_add_f32_e32 v24, 1.0, v24
	v_mul_f32_e32 v19, v52, v19
	v_rcp_f32_e32 v23, v23
	v_rcp_f32_e32 v24, v24
	v_mul_f32_e32 v21, v46, v21
	v_mul_f32_e32 v22, v47, v22
	v_mul_f32_e32 v17, 0x3c000000, v17
	v_mul_f32_e32 v25, 0x3c000000, v18
	v_mov_b32_e32 v18, 0
	v_mul_f32_e32 v27, 0x3c000000, v19
	v_cvt_pk_fp8_f32 v18, v17, v25
	v_mul_f32_e32 v17, 0x3c000000, v21
	v_mul_f32_e32 v21, 0x3c000000, v22
	v_mov_b32_e32 v19, 0
	v_cvt_pk_fp8_f32 v19, v17, v21
	v_mul_f32_e32 v20, v53, v20
	v_mul_f32_e32 v23, v48, v23
	v_mul_f32_e32 v24, v49, v24
	v_mul_f32_e32 v20, 0x3c000000, v20
	v_cvt_pk_fp8_f32 v18, v27, v20 op_sel:[0,0,1]
	v_mul_f32_e32 v17, 0x3c000000, v23
	v_mul_f32_e32 v20, 0x3c000000, v24
	v_cvt_pk_fp8_f32 v19, v17, v20 op_sel:[0,0,1]
	global_store_dwordx2 v[6:7], v[18:19], off offset:128
	s_cbranch_execnz .LBB0_1239

.LBB0_1239:
	v_add_u32_e32 v6, 0xa0, v4
	v_mad_i64_i32 v[10:11], s[52:53], v6, s73, 0
	v_lshl_add_u64 v[8:9], v[10:11], 1, s[12:13]
	v_lshl_add_u64 v[8:9], v[2:3], 1, v[8:9]
	v_ashrrev_i32_e32 v7, 31, v6
	v_lshlrev_b64 v[6:7], 11, v[6:7]
	v_lshl_add_u64 v[6:7], s[4:5], 0, v[6:7]
	s_and_b64 vcc, exec, s[0:1]
	v_lshl_add_u64 v[6:7], v[6:7], 0, v[2:3]
	v_lshlrev_b32_e32 v18, 16, v246
	v_and_b32_e32 v17, 0xffff0000, v246
	v_lshlrev_b32_e32 v16, 16, v247
	v_and_b32_e32 v15, 0xffff0000, v247
	v_lshlrev_b32_e32 v14, 16, v248
	v_and_b32_e32 v13, 0xffff0000, v248
	v_lshlrev_b32_e32 v12, 16, v249
	v_and_b32_e32 v5, 0xffff0000, v249
	s_cbranch_vccnz .LBB0_1268
	v_mul_f32_e32 v19, 0xbfb8aa3b, v18
	v_mul_f32_e32 v20, 0xbfb8aa3b, v17
	v_exp_f32_e32 v19, v19
	v_mul_f32_e32 v21, 0xbfb8aa3b, v16
	v_exp_f32_e32 v20, v20
	v_mul_f32_e32 v23, 0xbfb8aa3b, v14
	v_mul_f32_e32 v24, 0xbfb8aa3b, v13
	v_exp_f32_e32 v21, v21
	v_exp_f32_e32 v23, v23
	v_exp_f32_e32 v24, v24
	v_mul_f32_e32 v22, 0xbfb8aa3b, v15
	v_add_f32_e32 v19, 1.0, v19
	v_add_f32_e32 v20, 1.0, v20
	v_exp_f32_e32 v22, v22
	v_mul_f32_e32 v25, 0xbfb8aa3b, v12
	v_mul_f32_e32 v27, 0xbfb8aa3b, v5
	v_rcp_f32_e32 v19, v19
	v_rcp_f32_e32 v20, v20
	v_add_f32_e32 v21, 1.0, v21
	v_add_f32_e32 v23, 1.0, v23
	v_add_f32_e32 v24, 1.0, v24
	v_exp_f32_e32 v25, v25
	v_exp_f32_e32 v27, v27
	v_rcp_f32_e32 v21, v21
	v_rcp_f32_e32 v23, v23
	v_rcp_f32_e32 v24, v24
	v_add_f32_e32 v22, 1.0, v22
	v_mul_f32_e32 v19, v74, v19
	v_mul_f32_e32 v20, v75, v20
	v_rcp_f32_e32 v22, v22
	v_add_f32_e32 v25, 1.0, v25
	v_add_f32_e32 v27, 1.0, v27
	v_mul_f32_e32 v21, v76, v21
	v_rcp_f32_e32 v25, v25
	v_rcp_f32_e32 v27, v27
	v_mul_f32_e32 v23, v70, v23
	v_mul_f32_e32 v24, v71, v24
	v_mul_f32_e32 v19, 0x3c000000, v19
	v_mul_f32_e32 v28, 0x3c000000, v20
	v_mov_b32_e32 v20, 0
	v_mul_f32_e32 v29, 0x3c000000, v21
	v_cvt_pk_fp8_f32 v20, v19, v28
	v_mul_f32_e32 v19, 0x3c000000, v23
	v_mul_f32_e32 v23, 0x3c000000, v24
	v_mov_b32_e32 v21, 0
	v_cvt_pk_fp8_f32 v21, v19, v23
	v_mul_f32_e32 v22, v77, v22
	v_mul_f32_e32 v25, v72, v25
	v_mul_f32_e32 v27, v73, v27
	v_mul_f32_e32 v22, 0x3c000000, v22
	v_cvt_pk_fp8_f32 v20, v29, v22 op_sel:[0,0,1]
	v_mul_f32_e32 v19, 0x3c000000, v25
	v_mul_f32_e32 v22, 0x3c000000, v27
	v_cvt_pk_fp8_f32 v21, v19, v22 op_sel:[0,0,1]
	global_store_dwordx2 v[6:7], v[20:21], off
	v_lshl_add_u64 v[10:11], v[10:11], 1, s[10:11]
	s_cbranch_execnz .LBB0_1242

.LBB0_1242:
	s_and_b64 vcc, exec, s[0:1]
	v_lshlrev_b32_e32 v16, 16, v250
	v_and_b32_e32 v15, 0xffff0000, v250
	v_lshlrev_b32_e32 v14, 16, v251
	v_and_b32_e32 v13, 0xffff0000, v251
	v_lshlrev_b32_e32 v12, 16, v252
	v_and_b32_e32 v9, 0xffff0000, v252
	v_lshlrev_b32_e32 v8, 16, v253
	v_and_b32_e32 v5, 0xffff0000, v253
	s_cbranch_vccnz .LBB0_1269
	v_mul_f32_e32 v17, 0xbfb8aa3b, v16
	v_mul_f32_e32 v18, 0xbfb8aa3b, v15
	v_exp_f32_e32 v17, v17
	v_mul_f32_e32 v19, 0xbfb8aa3b, v14
	v_exp_f32_e32 v18, v18
	v_mul_f32_e32 v21, 0xbfb8aa3b, v12
	v_mul_f32_e32 v22, 0xbfb8aa3b, v9
	v_exp_f32_e32 v19, v19
	v_exp_f32_e32 v21, v21
	v_exp_f32_e32 v22, v22
	v_mul_f32_e32 v20, 0xbfb8aa3b, v13
	v_add_f32_e32 v17, 1.0, v17
	v_add_f32_e32 v18, 1.0, v18
	v_exp_f32_e32 v20, v20
	v_mul_f32_e32 v23, 0xbfb8aa3b, v8
	v_mul_f32_e32 v24, 0xbfb8aa3b, v5
	v_rcp_f32_e32 v17, v17
	v_rcp_f32_e32 v18, v18
	v_add_f32_e32 v19, 1.0, v19
	v_add_f32_e32 v21, 1.0, v21
	v_add_f32_e32 v22, 1.0, v22
	v_exp_f32_e32 v23, v23
	v_exp_f32_e32 v24, v24
	v_rcp_f32_e32 v19, v19
	v_rcp_f32_e32 v21, v21
	v_rcp_f32_e32 v22, v22
	v_add_f32_e32 v20, 1.0, v20
	v_mul_f32_e32 v17, v42, v17
	v_mul_f32_e32 v18, v43, v18
	v_rcp_f32_e32 v20, v20
	v_add_f32_e32 v23, 1.0, v23
	v_add_f32_e32 v24, 1.0, v24
	v_mul_f32_e32 v19, v44, v19
	v_rcp_f32_e32 v23, v23
	v_rcp_f32_e32 v24, v24
	v_mul_f32_e32 v21, v38, v21
	v_mul_f32_e32 v22, v39, v22
	v_mul_f32_e32 v17, 0x3c000000, v17
	v_mul_f32_e32 v25, 0x3c000000, v18
	v_mov_b32_e32 v18, 0
	v_mul_f32_e32 v27, 0x3c000000, v19
	v_cvt_pk_fp8_f32 v18, v17, v25
	v_mul_f32_e32 v17, 0x3c000000, v21
	v_mul_f32_e32 v21, 0x3c000000, v22
	v_mov_b32_e32 v19, 0
	v_cvt_pk_fp8_f32 v19, v17, v21
	v_mul_f32_e32 v20, v45, v20
	v_mul_f32_e32 v23, v40, v23
	v_mul_f32_e32 v24, v41, v24
	v_mul_f32_e32 v20, 0x3c000000, v20
	v_cvt_pk_fp8_f32 v18, v27, v20 op_sel:[0,0,1]
	v_mul_f32_e32 v17, 0x3c000000, v23
	v_mul_f32_e32 v20, 0x3c000000, v24
	v_cvt_pk_fp8_f32 v19, v17, v20 op_sel:[0,0,1]
	global_store_dwordx2 v[6:7], v[18:19], off offset:128
	s_cbranch_execnz .LBB0_1245
